# baseline (speedup 1.0000x reference)
.LBB2_1:
	s_add_i32 s13, s3, -4
	s_and_b32 s13, s13, 4
	s_mulk_i32 s13, 0x2400
	v_add_u32_e32 v124, s13, v120
	ds_read_b128 v[96:99], v124
	ds_read_b128 v[126:129], v124 offset:32
	ds_read_b128 v[130:133], v124 offset:4608
	ds_read_b128 v[134:137], v124 offset:4640
	v_lshl_add_u64 v[118:119], v[108:109], 0, s[4:5]
	v_add_co_u32_e32 v150, vcc, s12, v118
	s_waitcnt vmcnt(7) lgkmcnt(3)
	v_mfma_f32_32x32x16_f16 v[48:63], v[96:99], v[88:91], 0
	v_mov_b32_e32 v125, v116
	v_lshl_add_u64 v[116:117], v[110:111], 0, s[4:5]
	v_addc_co_u32_e32 v151, vcc, 0, v119, vcc
	v_mov_b32_e32 v123, v100
	v_lshl_add_u64 v[102:103], v[112:113], 0, s[6:7]
	v_lshl_add_u64 v[100:101], v[114:115], 0, s[6:7]
	s_waitcnt lgkmcnt(1)
	v_mfma_f32_32x32x16_f16 v[32:47], v[130:133], v[88:91], 0
	v_add_co_u32_e32 v158, vcc, s12, v116
	s_and_b32 s13, s3, 4
	s_nop 0
	v_addc_co_u32_e32 v159, vcc, 0, v117, vcc
	s_mulk_i32 s13, 0x2400
	v_add_u32_e32 v218, s13, v121
	s_waitcnt vmcnt(5)
	v_mfma_f32_32x32x16_f16 v[48:63], v[96:99], v[92:95], v[48:63]
	s_add_u32 s6, s6, 0x80
	s_addc_u32 s7, s7, 0
	s_add_i32 s3, s3, 4
	s_add_u32 s4, s4, 0x2000
	s_addc_u32 s5, s5, 0
	s_cmpk_eq_i32 s6, 0x780
	v_mfma_f32_32x32x16_f16 v[32:47], v[130:133], v[92:95], v[32:47]
	ds_read_b128 v[96:99], v124 offset:9216
	ds_read_b128 v[130:133], v124 offset:9248
	s_waitcnt lgkmcnt(1)
	v_mfma_f32_32x32x16_f16 v[48:63], v[96:99], v[88:91], v[48:63]
	ds_read_b128 v[138:141], v124 offset:13824
	ds_read_b128 v[96:99], v124 offset:13856
	s_waitcnt lgkmcnt(1)
	v_mfma_f32_32x32x16_f16 v[32:47], v[138:141], v[88:91], v[32:47]
	v_mfma_f32_32x32x16_f16 v[48:63], v[126:129], v[80:83], v[48:63]
	v_mfma_f32_32x32x16_f16 v[32:47], v[134:137], v[80:83], v[32:47]
	s_waitcnt vmcnt(4)
	v_mfma_f32_32x32x16_f16 v[48:63], v[126:129], v[84:87], v[48:63]
	v_mfma_f32_32x32x16_f16 v[32:47], v[134:137], v[84:87], v[32:47]
	v_mfma_f32_32x32x16_f16 v[48:63], v[130:133], v[80:83], v[48:63]
	s_waitcnt lgkmcnt(0)
	v_mfma_f32_32x32x16_f16 v[32:47], v[96:99], v[80:83], v[32:47]
	ds_read_b128 v[96:99], v124 offset:64
	ds_read_b128 v[126:129], v124 offset:96
	ds_read_b128 v[130:133], v124 offset:4672
	ds_read_b128 v[134:137], v124 offset:4704
	global_load_dwordx4 v[116:119], v[102:103], off offset:128
	global_load_dwordx4 v[138:141], v[100:101], off offset:128
	v_add_co_u32_e32 v102, vcc, s1, v102
	s_waitcnt vmcnt(5) lgkmcnt(3)
	v_mfma_f32_32x32x16_f16 v[48:63], v[96:99], v[72:75], v[48:63]
	v_addc_co_u32_e32 v103, vcc, 0, v103, vcc
	v_add_co_u32_e32 v100, vcc, s1, v100
	s_nop 1
	v_addc_co_u32_e32 v101, vcc, 0, v101, vcc
	s_waitcnt lgkmcnt(1)
	v_mfma_f32_32x32x16_f16 v[32:47], v[130:133], v[72:75], v[32:47]
	s_waitcnt vmcnt(3)
	v_mfma_f32_32x32x16_f16 v[48:63], v[96:99], v[76:79], v[48:63]
	v_mfma_f32_32x32x16_f16 v[32:47], v[130:133], v[76:79], v[32:47]
	ds_read_b128 v[96:99], v124 offset:9280
	ds_read_b128 v[130:133], v124 offset:9312
	s_waitcnt lgkmcnt(1)
	v_mfma_f32_32x32x16_f16 v[48:63], v[96:99], v[72:75], v[48:63]
	ds_read_b128 v[96:99], v124 offset:13888
	ds_read_b128 v[142:145], v124 offset:13920
	global_load_dwordx4 v[146:149], v[150:151], off offset:-4096
	s_nop 0
	global_load_dwordx4 v[150:153], v[150:151], off
	s_nop 0
	global_load_dwordx4 v[154:157], v[158:159], off offset:-4096
	s_nop 0
	global_load_dwordx4 v[158:161], v[158:159], off
	s_nop 0
	global_load_dwordx4 v[162:165], v[102:103], off offset:128
	global_load_dwordx4 v[166:169], v[100:101], off offset:128
	ds_read_b128 v[170:173], v124 offset:23040
	ds_read_b128 v[174:177], v124 offset:18432
	ds_read_b128 v[178:181], v124 offset:18464
	ds_read_b128 v[182:185], v124 offset:27648
	ds_read_b128 v[186:189], v124 offset:27680
	v_mfma_f32_32x32x16_f16 v[48:63], v[126:129], v[64:67], v[48:63]
	s_waitcnt lgkmcnt(6)
	v_mfma_f32_32x32x16_f16 v[32:47], v[96:99], v[72:75], v[32:47]
	s_waitcnt vmcnt(8)
	v_mfma_f32_32x32x16_f16 v[48:63], v[126:129], v[68:71], v[48:63]
	ds_read_b128 v[126:129], v124 offset:23072
	ds_read_b128 v[190:193], v124 offset:32256
	ds_read_b128 v[194:197], v124 offset:32288
	ds_read_b128 v[198:201], v124 offset:18496
	ds_read_b128 v[202:205], v124 offset:18528
	ds_read_b128 v[206:209], v124 offset:27712
	ds_read_b128 v[100:103], v124 offset:27744
	v_mfma_f32_32x32x16_f16 v[32:47], v[134:137], v[64:67], v[32:47]
	v_mfma_f32_32x32x16_f16 v[48:63], v[130:133], v[64:67], v[48:63]
	v_mfma_f32_32x32x16_f16 v[32:47], v[134:137], v[68:71], v[32:47]
	ds_read_b128 v[134:137], v124 offset:23104
	ds_read_b128 v[210:213], v124 offset:23136
	ds_read_b128 v[214:217], v124 offset:32320
	ds_read_b128 v[96:99], v124 offset:32352
	s_waitcnt vmcnt(7)
	ds_write_b128 v218, v[116:119] offset:18432
	s_waitcnt vmcnt(6)
	ds_write_b128 v218, v[138:141] offset:27648
	s_waitcnt vmcnt(5)
	ds_write_b128 v218, v[146:149]
	s_waitcnt vmcnt(4)
	ds_write_b128 v218, v[150:153] offset:4608
	s_waitcnt vmcnt(3)
	ds_write_b128 v218, v[154:157] offset:9216
	s_waitcnt vmcnt(2)
	ds_write_b128 v218, v[158:161] offset:13824
	s_waitcnt vmcnt(1)
	ds_write_b128 v218, v[162:165] offset:23040
	v_max_f32_e32 v116, v49, v49
	v_max_f32_e32 v117, v48, v48
	s_waitcnt lgkmcnt(14)
	v_mfma_f32_32x32x16_f16 v[32:47], v[142:145], v[64:67], v[32:47]
	v_max_f32_e32 v116, v117, v116
	v_max3_f32 v116, v116, v50, v51
	v_max3_f32 v116, v116, v52, v53
	v_max3_f32 v116, v116, v54, v55
	v_max3_f32 v116, v116, v56, v57
	v_max3_f32 v116, v116, v58, v59
	v_max3_f32 v116, v116, v60, v61
	v_max3_f32 v116, v116, v62, v63
	s_nop 3
	v_max3_f32 v116, v116, v32, v33
	v_max3_f32 v116, v116, v34, v35
	v_max3_f32 v116, v116, v36, v37
	v_max3_f32 v116, v116, v38, v39
	v_max3_f32 v116, v116, v40, v41
	v_max3_f32 v116, v116, v42, v43
	v_max3_f32 v116, v116, v44, v45
	v_max3_f32 v116, v116, v46, v47
	ds_bpermute_b32 v117, v107, v116
	s_waitcnt vmcnt(0)
	ds_write_b128 v218, v[166:169] offset:32256
	s_waitcnt lgkmcnt(0)
	s_barrier
	v_max3_f32 v116, v125, v116, v117
	v_sub_f32_e32 v117, v125, v116
	v_fmamk_f32 v119, v116, 0xb9b8aa3b, v122
	v_mul_f32_e32 v117, 0x39b8aa3b, v117
	v_fmamk_f32 v48, v48, 0x39b8aa3b, v119
	v_fmamk_f32 v49, v49, 0x39b8aa3b, v119
	v_fmamk_f32 v50, v50, 0x39b8aa3b, v119
	v_fmamk_f32 v51, v51, 0x39b8aa3b, v119
	v_fmamk_f32 v52, v52, 0x39b8aa3b, v119
	v_fmamk_f32 v53, v53, 0x39b8aa3b, v119
	v_fmamk_f32 v54, v54, 0x39b8aa3b, v119
	v_fmamk_f32 v55, v55, 0x39b8aa3b, v119
	v_exp_f32_e32 v118, v117
	v_exp_f32_e32 v117, v48
	v_exp_f32_e32 v140, v49
	v_exp_f32_e32 v124, v50
	v_exp_f32_e32 v125, v51
	v_exp_f32_e32 v130, v52
	v_exp_f32_e32 v131, v53
	v_exp_f32_e32 v132, v54
	v_exp_f32_e32 v133, v55
	v_mul_f32_e32 v30, v118, v30
	v_mul_f32_e32 v31, v118, v31
	v_mul_f32_e32 v28, v118, v28
	v_mul_f32_e32 v29, v118, v29
	v_mul_f32_e32 v26, v118, v26
	v_mul_f32_e32 v27, v118, v27
	v_mul_f32_e32 v24, v118, v24
	v_mul_f32_e32 v25, v118, v25
	v_mul_f32_e32 v22, v118, v22
	v_mul_f32_e32 v23, v118, v23
	v_mul_f32_e32 v20, v118, v20
	v_mul_f32_e32 v21, v118, v21
	v_mul_f32_e32 v18, v118, v18
	v_mul_f32_e32 v19, v118, v19
	v_mul_f32_e32 v16, v118, v16
	v_mul_f32_e32 v17, v118, v17
	v_mul_f32_e32 v14, v118, v14
	v_mul_f32_e32 v15, v118, v15
	v_mul_f32_e32 v12, v118, v12
	v_mul_f32_e32 v13, v118, v13
	v_mul_f32_e32 v10, v118, v10
	v_mul_f32_e32 v11, v118, v11
	v_mul_f32_e32 v8, v118, v8
	v_mul_f32_e32 v9, v118, v9
	v_mul_f32_e32 v6, v118, v6
	v_mul_f32_e32 v7, v118, v7
	v_mul_f32_e32 v4, v118, v4
	v_mul_f32_e32 v5, v118, v5
	v_mul_f32_e32 v2, v118, v2
	v_mul_f32_e32 v3, v118, v3
	v_mul_f32_e32 v0, v118, v0
	v_mul_f32_e32 v1, v118, v1
	v_cvt_pk_f16_f32 v48, v117, v140
	v_cvt_pk_f16_f32 v49, v124, v125
	v_cvt_pk_f16_f32 v50, v130, v131
	v_cvt_pk_f16_f32 v51, v132, v133
	s_nop 1
	v_mfma_f32_32x32x16_f16 v[16:31], v[174:177], v[48:51], v[16:31]
	v_mfma_f32_32x32x16_f16 v[0:15], v[170:173], v[48:51], v[0:15]
	v_fma_mixlo_f16 v53, v124, 1.0, -v49 op_sel_hi:[0,0,1]
	v_fma_mixhi_f16 v53, v125, 1.0, -v49 op_sel:[0,0,1] op_sel_hi:[0,0,1]
	v_fma_mixlo_f16 v54, v130, 1.0, -v50 op_sel_hi:[0,0,1]
	v_fma_mixhi_f16 v54, v131, 1.0, -v50 op_sel:[0,0,1] op_sel_hi:[0,0,1]
	v_fma_mixlo_f16 v55, v132, 1.0, -v51 op_sel_hi:[0,0,1]
	v_fma_mixhi_f16 v55, v133, 1.0, -v51 op_sel:[0,0,1] op_sel_hi:[0,0,1]
	v_fma_mixlo_f16 v52, v117, 1.0, -v48 op_sel_hi:[0,0,1]
	v_fma_mixhi_f16 v52, v140, 1.0, -v48 op_sel:[0,0,1] op_sel_hi:[0,0,1]
	v_fmamk_f32 v56, v56, 0x39b8aa3b, v119
	v_fmamk_f32 v57, v57, 0x39b8aa3b, v119
	v_mfma_f32_32x32x16_f16 v[16:31], v[174:177], v[52:55], v[16:31]
	v_fmamk_f32 v58, v58, 0x39b8aa3b, v119
	v_fmamk_f32 v59, v59, 0x39b8aa3b, v119
	v_exp_f32_e32 v138, v56
	v_exp_f32_e32 v139, v57
	v_exp_f32_e32 v56, v58
	v_exp_f32_e32 v57, v59
	v_mfma_f32_32x32x16_f16 v[0:15], v[170:173], v[52:55], v[0:15]
	v_fmamk_f32 v52, v60, 0x39b8aa3b, v119
	v_fmamk_f32 v53, v61, 0x39b8aa3b, v119
	v_fmamk_f32 v54, v62, 0x39b8aa3b, v119
	v_fmamk_f32 v55, v63, 0x39b8aa3b, v119
	v_exp_f32_e32 v58, v52
	v_exp_f32_e32 v59, v53
	v_exp_f32_e32 v60, v54
	v_mfma_f32_32x32x16_f16 v[16:31], v[182:185], v[48:51], v[16:31]
	v_exp_f32_e32 v61, v55
	v_fmamk_f32 v32, v32, 0x39b8aa3b, v119
	v_fmamk_f32 v33, v33, 0x39b8aa3b, v119
	v_fmamk_f32 v34, v34, 0x39b8aa3b, v119
	v_mfma_f32_32x32x16_f16 v[0:15], v[190:193], v[48:51], v[0:15]
	v_cvt_pk_f16_f32 v48, v138, v139
	v_cvt_pk_f16_f32 v49, v56, v57
	v_cvt_pk_f16_f32 v50, v58, v59
	v_cvt_pk_f16_f32 v51, v60, v61
	s_nop 1
	v_mfma_f32_32x32x16_f16 v[16:31], v[178:181], v[48:51], v[16:31]
	v_fma_mixlo_f16 v53, v56, 1.0, -v49 op_sel_hi:[0,0,1]
	v_fma_mixhi_f16 v53, v57, 1.0, -v49 op_sel:[0,0,1] op_sel_hi:[0,0,1]
	v_mfma_f32_32x32x16_f16 v[0:15], v[126:129], v[48:51], v[0:15]
	v_fma_mixlo_f16 v54, v58, 1.0, -v50 op_sel_hi:[0,0,1]
	v_fma_mixhi_f16 v54, v59, 1.0, -v50 op_sel:[0,0,1] op_sel_hi:[0,0,1]
	v_fma_mixlo_f16 v55, v60, 1.0, -v51 op_sel_hi:[0,0,1]
	v_fma_mixhi_f16 v55, v61, 1.0, -v51 op_sel:[0,0,1] op_sel_hi:[0,0,1]
	v_fma_mixlo_f16 v52, v138, 1.0, -v48 op_sel_hi:[0,0,1]
	v_fma_mixhi_f16 v52, v139, 1.0, -v48 op_sel:[0,0,1] op_sel_hi:[0,0,1]
	v_fmamk_f32 v35, v35, 0x39b8aa3b, v119
	v_fmamk_f32 v36, v36, 0x39b8aa3b, v119
	v_mfma_f32_32x32x16_f16 v[16:31], v[178:181], v[52:55], v[16:31]
	v_fmamk_f32 v37, v37, 0x39b8aa3b, v119
	v_fmamk_f32 v38, v38, 0x39b8aa3b, v119
	v_fmamk_f32 v39, v39, 0x39b8aa3b, v119
	v_fmamk_f32 v62, v40, 0x39b8aa3b, v119
	v_fmamk_f32 v63, v41, 0x39b8aa3b, v119
	v_exp_f32_e32 v40, v34
	v_exp_f32_e32 v41, v35
	v_mfma_f32_32x32x16_f16 v[0:15], v[126:129], v[52:55], v[0:15]
	v_exp_f32_e32 v126, v32
	v_exp_f32_e32 v127, v33
	v_exp_f32_e32 v52, v36
	v_exp_f32_e32 v53, v37
	v_exp_f32_e32 v54, v38
	v_exp_f32_e32 v55, v39
	v_mfma_f32_32x32x16_f16 v[16:31], v[186:189], v[48:51], v[16:31]
	v_cvt_pk_f16_f32 v32, v126, v127
	v_cvt_pk_f16_f32 v33, v40, v41
	v_cvt_pk_f16_f32 v34, v52, v53
	v_cvt_pk_f16_f32 v35, v54, v55
	v_mfma_f32_32x32x16_f16 v[0:15], v[194:197], v[48:51], v[0:15]
	s_nop 0
	v_mfma_f32_32x32x16_f16 v[16:31], v[198:201], v[32:35], v[16:31]
	v_fma_mixlo_f16 v37, v40, 1.0, -v33 op_sel_hi:[0,0,1]
	v_fma_mixhi_f16 v37, v41, 1.0, -v33 op_sel:[0,0,1] op_sel_hi:[0,0,1]
	v_fma_mixlo_f16 v38, v52, 1.0, -v34 op_sel_hi:[0,0,1]
	v_fma_mixhi_f16 v38, v53, 1.0, -v34 op_sel:[0,0,1] op_sel_hi:[0,0,1]
	v_fma_mixlo_f16 v39, v54, 1.0, -v35 op_sel_hi:[0,0,1]
	v_fma_mixhi_f16 v39, v55, 1.0, -v35 op_sel:[0,0,1] op_sel_hi:[0,0,1]
	v_mfma_f32_32x32x16_f16 v[0:15], v[134:137], v[32:35], v[0:15]
	v_fma_mixlo_f16 v36, v126, 1.0, -v32 op_sel_hi:[0,0,1]
	v_fma_mixhi_f16 v36, v127, 1.0, -v32 op_sel:[0,0,1] op_sel_hi:[0,0,1]
	v_exp_f32_e32 v50, v62
	v_exp_f32_e32 v51, v63
	v_fmamk_f32 v42, v42, 0x39b8aa3b, v119
	v_fmamk_f32 v43, v43, 0x39b8aa3b, v119
	v_fmamk_f32 v44, v44, 0x39b8aa3b, v119
	v_fmamk_f32 v45, v45, 0x39b8aa3b, v119
	v_mfma_f32_32x32x16_f16 v[16:31], v[198:201], v[36:39], v[16:31]
	v_fmamk_f32 v46, v46, 0x39b8aa3b, v119
	v_fmac_f32_e32 v119, 0x39b8aa3b, v47
	v_exp_f32_e32 v42, v42
	v_exp_f32_e32 v43, v43
	v_exp_f32_e32 v44, v44
	v_exp_f32_e32 v45, v45
	v_exp_f32_e32 v46, v46
	v_mfma_f32_32x32x16_f16 v[0:15], v[134:137], v[36:39], v[0:15]
	v_exp_f32_e32 v47, v119
	v_add_f32_e32 v48, 0, v117
	v_cvt_pk_f16_f32 v37, v42, v43
	v_cvt_pk_f16_f32 v38, v44, v45
	v_cvt_pk_f16_f32 v39, v46, v47
	v_mfma_f32_32x32x16_f16 v[16:31], v[206:209], v[32:35], v[16:31]
	v_add_f32_e32 v117, v48, v140
	v_add_f32_e32 v117, v117, v124
	v_cvt_pk_f16_f32 v36, v50, v51
	v_mfma_f32_32x32x16_f16 v[0:15], v[214:217], v[32:35], v[0:15]
	v_add_f32_e32 v117, v117, v125
	v_mfma_f32_32x32x16_f16 v[16:31], v[202:205], v[36:39], v[16:31]
	v_add_f32_e32 v117, v117, v130
	v_fma_mixlo_f16 v33, v42, 1.0, -v37 op_sel_hi:[0,0,1]
	v_fma_mixhi_f16 v33, v43, 1.0, -v37 op_sel:[0,0,1] op_sel_hi:[0,0,1]
	v_fma_mixlo_f16 v34, v44, 1.0, -v38 op_sel_hi:[0,0,1]
	v_fma_mixhi_f16 v34, v45, 1.0, -v38 op_sel:[0,0,1] op_sel_hi:[0,0,1]
	v_fma_mixlo_f16 v35, v46, 1.0, -v39 op_sel_hi:[0,0,1]
	v_fma_mixhi_f16 v35, v47, 1.0, -v39 op_sel:[0,0,1] op_sel_hi:[0,0,1]
	v_fma_mixlo_f16 v32, v50, 1.0, -v36 op_sel_hi:[0,0,1]
	v_fma_mixhi_f16 v32, v51, 1.0, -v36 op_sel:[0,0,1] op_sel_hi:[0,0,1]
	v_mfma_f32_32x32x16_f16 v[0:15], v[210:213], v[36:39], v[0:15]
	v_add_f32_e32 v48, v117, v131
	v_add_f32_e32 v48, v48, v132
	v_add_f32_e32 v48, v48, v133
	v_add_f32_e32 v48, v48, v138
	v_add_f32_e32 v48, v48, v139
	v_add_f32_e32 v48, v48, v56
	v_add_f32_e32 v48, v48, v57
	v_mfma_f32_32x32x16_f16 v[16:31], v[202:205], v[32:35], v[16:31]
	v_mfma_f32_32x32x16_f16 v[0:15], v[210:213], v[32:35], v[0:15]
	v_add_f32_e32 v32, v48, v58
	v_add_f32_e32 v32, v32, v59
	v_add_f32_e32 v32, v32, v60
	v_add_f32_e32 v32, v32, v61
	v_add_f32_e32 v32, v32, v126
	v_add_f32_e32 v32, v32, v127
	v_add_f32_e32 v32, v32, v40
	v_add_f32_e32 v32, v32, v41
	v_add_f32_e32 v32, v32, v52
	v_add_f32_e32 v32, v32, v53
	v_add_f32_e32 v32, v32, v54
	v_add_f32_e32 v32, v32, v55
	v_add_f32_e32 v32, v32, v50
	v_mfma_f32_32x32x16_f16 v[16:31], v[100:103], v[36:39], v[16:31]
	v_add_f32_e32 v32, v32, v51
	v_add_f32_e32 v32, v32, v42
	v_add_f32_e32 v32, v32, v43
	v_add_f32_e32 v32, v32, v44
	v_add_f32_e32 v32, v32, v45
	v_add_f32_e32 v32, v32, v46
	v_add_f32_e32 v100, v32, v47
	v_mfma_f32_32x32x16_f16 v[0:15], v[96:99], v[36:39], v[0:15]
	v_fmac_f32_e32 v100, v123, v118
	s_cbranch_scc0 .LBB2_1
	ds_read_b128 v[48:51], v120 offset:36864
	ds_read_b128 v[52:55], v120 offset:36896
	v_add_u32_e32 v102, 0xea00, v120
	s_ashr_i32 s0, s0, 3
	s_ashr_i32 s1, s0, 31
	s_waitcnt lgkmcnt(1)
	v_mfma_f32_32x32x16_f16 v[32:47], v[48:51], v[88:91], 0
	s_lshl_b64 s[0:1], s[0:1], 10
	v_mfma_f32_32x32x16_f16 v[32:47], v[48:51], v[92:95], v[32:47]
	ds_read_b128 v[48:51], v120 offset:46080
	ds_read_b128 v[56:59], v120 offset:46112
	s_waitcnt lgkmcnt(1)
	v_mfma_f32_32x32x16_f16 v[32:47], v[48:51], v[88:91], v[32:47]
	v_mfma_f32_32x32x16_f16 v[32:47], v[52:55], v[80:83], v[32:47]
	v_mfma_f32_32x32x16_f16 v[32:47], v[52:55], v[84:87], v[32:47]
	ds_read_b128 v[48:51], v120 offset:36928
	ds_read_b128 v[52:55], v120 offset:36960
	s_waitcnt lgkmcnt(2)
	v_mfma_f32_32x32x16_f16 v[32:47], v[56:59], v[80:83], v[32:47]
	s_waitcnt lgkmcnt(1)
	v_mfma_f32_32x32x16_f16 v[32:47], v[48:51], v[72:75], v[32:47]
	v_mfma_f32_32x32x16_f16 v[32:47], v[48:51], v[76:79], v[32:47]
	ds_read_b128 v[48:51], v120 offset:46144
	ds_read_b128 v[56:59], v120 offset:46176
	ds_read_b128 v[96:99], v120 offset:41472
	ds_read_b128 v[108:111], v120 offset:41504
	s_waitcnt lgkmcnt(3)
	v_mfma_f32_32x32x16_f16 v[32:47], v[48:51], v[72:75], v[32:47]
	v_mfma_f32_32x32x16_f16 v[32:47], v[52:55], v[64:67], v[32:47]
	v_mfma_f32_32x32x16_f16 v[32:47], v[52:55], v[68:71], v[32:47]
	s_waitcnt lgkmcnt(2)
	v_mfma_f32_32x32x16_f16 v[32:47], v[56:59], v[64:67], v[32:47]
	s_waitcnt lgkmcnt(1)
	v_mfma_f32_32x32x16_f16 v[48:63], v[96:99], v[88:91], 0
	v_mfma_f32_32x32x16_f16 v[48:63], v[96:99], v[92:95], v[48:63]
	ds_read_b128 v[92:95], v120 offset:50688
	ds_read_b128 v[96:99], v120 offset:50720
	s_waitcnt lgkmcnt(1)
	v_mfma_f32_32x32x16_f16 v[48:63], v[92:95], v[88:91], v[48:63]
	v_mfma_f32_32x32x16_f16 v[48:63], v[108:111], v[80:83], v[48:63]
	v_mfma_f32_32x32x16_f16 v[48:63], v[108:111], v[84:87], v[48:63]
	s_waitcnt lgkmcnt(0)
	v_mfma_f32_32x32x16_f16 v[48:63], v[96:99], v[80:83], v[48:63]
	ds_read_b128 v[80:83], v120 offset:41536
	ds_read_b128 v[84:87], v120 offset:41568
	s_waitcnt lgkmcnt(1)
	v_mfma_f32_32x32x16_f16 v[48:63], v[80:83], v[72:75], v[48:63]
	v_mfma_f32_32x32x16_f16 v[48:63], v[80:83], v[76:79], v[48:63]
	ds_read_b128 v[76:79], v120 offset:50752
	ds_read_b128 v[80:83], v120 offset:50784
	s_waitcnt lgkmcnt(1)
	v_mfma_f32_32x32x16_f16 v[48:63], v[76:79], v[72:75], v[48:63]
	v_max_f32_e32 v72, v33, v33
	v_max_f32_e32 v73, v32, v32
	v_max_f32_e32 v72, v73, v72
	v_mfma_f32_32x32x16_f16 v[48:63], v[84:87], v[64:67], v[48:63]
	v_mfma_f32_32x32x16_f16 v[48:63], v[84:87], v[68:71], v[48:63]
	v_max3_f32 v68, v72, v34, v35
	v_max3_f32 v68, v68, v36, v37
	v_max3_f32 v68, v68, v38, v39
	v_max3_f32 v68, v68, v40, v41
	v_max3_f32 v68, v68, v42, v43
	v_max3_f32 v68, v68, v44, v45
	v_max3_f32 v68, v68, v46, v47
	s_waitcnt lgkmcnt(0)
	v_mfma_f32_32x32x16_f16 v[48:63], v[80:83], v[64:67], v[48:63]
	s_nop 11
	v_max3_f32 v64, v68, v48, v49
	v_max3_f32 v64, v64, v50, v51
	v_max3_f32 v64, v64, v52, v53
	v_max3_f32 v64, v64, v54, v55
	v_max3_f32 v64, v64, v56, v57
	v_max3_f32 v64, v64, v58, v59
	v_max3_f32 v64, v64, v60, v61
	v_max3_f32 v64, v64, v62, v63
	ds_bpermute_b32 v65, v107, v64
	v_mov_b32_e32 v68, 0x41000000
	s_waitcnt lgkmcnt(0)
	v_max3_f32 v65, v116, v64, v65
	v_fmac_f32_e32 v68, 0xb9b8aa3b, v65
	v_fmamk_f32 v32, v32, 0x39b8aa3b, v68
	v_sub_f32_e32 v64, v116, v65
	v_exp_f32_e32 v65, v32
	v_fmamk_f32 v32, v33, 0x39b8aa3b, v68
	v_exp_f32_e32 v101, v32
	v_fmamk_f32 v32, v34, 0x39b8aa3b, v68
	v_exp_f32_e32 v66, v32
	v_fmamk_f32 v32, v35, 0x39b8aa3b, v68
	v_exp_f32_e32 v67, v32
	v_fmamk_f32 v32, v36, 0x39b8aa3b, v68
	v_exp_f32_e32 v36, v32
	v_fmamk_f32 v32, v37, 0x39b8aa3b, v68
	v_exp_f32_e32 v37, v32
	v_fmamk_f32 v32, v38, 0x39b8aa3b, v68
	v_exp_f32_e32 v38, v32
	v_fmamk_f32 v32, v39, 0x39b8aa3b, v68
	v_exp_f32_e32 v39, v32
	v_fmamk_f32 v32, v40, 0x39b8aa3b, v68
	v_exp_f32_e32 v124, v32
	v_fmamk_f32 v32, v41, 0x39b8aa3b, v68
	v_exp_f32_e32 v125, v32
	v_fmamk_f32 v32, v42, 0x39b8aa3b, v68
	v_exp_f32_e32 v40, v32
	v_fmamk_f32 v32, v43, 0x39b8aa3b, v68
	v_exp_f32_e32 v41, v32
	v_fmamk_f32 v32, v44, 0x39b8aa3b, v68
	v_exp_f32_e32 v42, v32
	v_fmamk_f32 v32, v45, 0x39b8aa3b, v68
	v_exp_f32_e32 v43, v32
	v_fmamk_f32 v32, v46, 0x39b8aa3b, v68
	v_exp_f32_e32 v44, v32
	v_fmamk_f32 v32, v47, 0x39b8aa3b, v68
	v_exp_f32_e32 v45, v32
	v_fmamk_f32 v32, v48, 0x39b8aa3b, v68
	v_exp_f32_e32 v126, v32
	v_fmamk_f32 v32, v49, 0x39b8aa3b, v68
	v_exp_f32_e32 v127, v32
	v_fmamk_f32 v32, v50, 0x39b8aa3b, v68
	v_exp_f32_e32 v46, v32
	v_fmamk_f32 v32, v51, 0x39b8aa3b, v68
	v_exp_f32_e32 v47, v32
	v_fmamk_f32 v32, v52, 0x39b8aa3b, v68
	v_exp_f32_e32 v48, v32
	v_fmamk_f32 v32, v53, 0x39b8aa3b, v68
	v_exp_f32_e32 v49, v32
	v_fmamk_f32 v32, v54, 0x39b8aa3b, v68
	v_exp_f32_e32 v50, v32
	v_fmamk_f32 v32, v55, 0x39b8aa3b, v68
	v_exp_f32_e32 v51, v32
	v_fmamk_f32 v32, v56, 0x39b8aa3b, v68
	v_exp_f32_e32 v128, v32
	v_fmamk_f32 v32, v57, 0x39b8aa3b, v68
	v_exp_f32_e32 v129, v32
	v_fmamk_f32 v32, v58, 0x39b8aa3b, v68
	v_exp_f32_e32 v52, v32
	v_fmamk_f32 v32, v59, 0x39b8aa3b, v68
	v_exp_f32_e32 v53, v32
	v_fmamk_f32 v32, v60, 0x39b8aa3b, v68
	v_exp_f32_e32 v54, v32
	v_fmamk_f32 v32, v61, 0x39b8aa3b, v68
	v_exp_f32_e32 v55, v32
	v_fmamk_f32 v32, v62, 0x39b8aa3b, v68
	v_exp_f32_e32 v56, v32
	v_cvt_f16_f32_e32 v32, v65
	v_cvt_f16_f32_e32 v33, v101
	v_cvt_pk_f16_f32 v59, v66, v67
	v_cvt_pk_f16_f32 v60, v36, v37
	v_cvt_f32_f16_e32 v32, v32
	v_cvt_f32_f16_e32 v35, v33
	v_cvt_f32_f16_sdwa v33, v59 dst_sel:DWORD dst_unused:UNUSED_PAD src0_sel:WORD_1
	v_fmac_f32_e32 v68, 0x39b8aa3b, v63
	v_sub_f32_e32 v34, v65, v32
	v_cvt_f32_f16_e32 v32, v59
	v_sub_f32_e32 v35, v101, v35
	v_cvt_pk_f16_f32 v61, v38, v39
	v_exp_f32_e32 v57, v68
	v_pk_add_f32 v[32:33], v[66:67], v[32:33] neg_lo:[0,1] neg_hi:[0,1]
	v_cvt_pk_f16_f32 v68, v34, v35
	v_cvt_pk_f16_f32 v69, v32, v33
	v_cvt_f32_f16_e32 v32, v60
	v_cvt_f32_f16_sdwa v33, v60 dst_sel:DWORD dst_unused:UNUSED_PAD src0_sel:WORD_1
	v_cvt_f32_f16_e32 v34, v61
	v_cvt_f32_f16_sdwa v35, v61 dst_sel:DWORD dst_unused:UNUSED_PAD src0_sel:WORD_1
	v_mul_f32_e32 v64, 0x39b8aa3b, v64
	v_pk_add_f32 v[32:33], v[36:37], v[32:33] neg_lo:[0,1] neg_hi:[0,1]
	v_exp_f32_e32 v64, v64
	v_cvt_pk_f16_f32 v70, v32, v33
	v_pk_add_f32 v[32:33], v[38:39], v[34:35] neg_lo:[0,1] neg_hi:[0,1]
	v_cvt_f16_f32_e32 v62, v124
	v_cvt_pk_f16_f32 v71, v32, v33
	ds_read_b128 v[32:35], v120 offset:55296
	v_cvt_f16_f32_e32 v63, v125
	v_pk_mul_f32 v[30:31], v[64:65], v[30:31] op_sel_hi:[0,1]
	v_pk_mul_f32 v[28:29], v[64:65], v[28:29] op_sel_hi:[0,1]
	v_pk_mul_f32 v[26:27], v[64:65], v[26:27] op_sel_hi:[0,1]
	v_pk_mul_f32 v[24:25], v[64:65], v[24:25] op_sel_hi:[0,1]
	v_pk_mul_f32 v[22:23], v[64:65], v[22:23] op_sel_hi:[0,1]
	v_pk_mul_f32 v[20:21], v[64:65], v[20:21] op_sel_hi:[0,1]
	v_pk_mul_f32 v[18:19], v[64:65], v[18:19] op_sel_hi:[0,1]
	v_pk_mul_f32 v[16:17], v[64:65], v[16:17] op_sel_hi:[0,1]
	v_cvt_pk_f16_f32 v58, v65, v101
	v_cvt_f32_f16_e32 v62, v62
	v_cvt_f32_f16_e32 v75, v63
	s_waitcnt lgkmcnt(0)
	v_mfma_f32_32x32x16_f16 v[16:31], v[32:35], v[58:61], v[16:31]
	v_cvt_pk_f16_f32 v73, v40, v41
	v_sub_f32_e32 v74, v124, v62
	v_sub_f32_e32 v75, v125, v75
	v_cvt_f32_f16_e32 v62, v73
	v_cvt_f32_f16_sdwa v63, v73 dst_sel:DWORD dst_unused:UNUSED_PAD src0_sel:WORD_1
	v_cvt_pk_f16_f32 v76, v74, v75
	v_cvt_pk_f16_f32 v74, v42, v43
	v_cvt_f32_f16_e32 v78, v74
	v_cvt_f32_f16_sdwa v79, v74 dst_sel:DWORD dst_unused:UNUSED_PAD src0_sel:WORD_1
	v_cvt_pk_f16_f32 v75, v44, v45
	v_cvt_f32_f16_e32 v80, v75
	v_cvt_f32_f16_sdwa v81, v75 dst_sel:DWORD dst_unused:UNUSED_PAD src0_sel:WORD_1
	v_mfma_f32_32x32x16_f16 v[16:31], v[32:35], v[68:71], v[16:31]
	v_add_f32_e64 v62, v40, -v62
	v_add_f32_e64 v63, v41, -v63
	v_mul_f32_e64 v14, v64, v14
	v_mul_f32_e64 v15, v64, v15
	v_cvt_pk_f16_f32 v77, v62, v63
	v_pk_add_f32 v[62:63], v[42:43], v[78:79] neg_lo:[0,1] neg_hi:[0,1]
	v_pk_mul_f32 v[12:13], v[64:65], v[12:13] op_sel_hi:[0,1]
	v_cvt_pk_f16_f32 v78, v62, v63
	v_pk_add_f32 v[62:63], v[44:45], v[80:81] neg_lo:[0,1] neg_hi:[0,1]
	ds_read_b128 v[80:83], v120 offset:55328
	ds_read_b128 v[84:87], v120 offset:64512
	ds_read_b128 v[88:91], v120 offset:64544
	s_waitcnt lgkmcnt(1)
	v_mfma_f32_32x32x16_f16 v[16:31], v[84:87], v[58:61], v[16:31]
	ds_read_b128 v[92:95], v120 offset:59904
	ds_read_b128 v[96:99], v120 offset:59936
	v_cvt_pk_f16_f32 v79, v62, v63
	v_add_u32_e32 v63, 0xea20, v120
	v_cvt_f16_f32_e32 v62, v126
	ds_read_b128 v[108:111], v102 offset:9216
	ds_read_b128 v[112:115], v63 offset:9216
	v_cvt_f16_f32_e32 v63, v127
	v_pk_mul_f32 v[10:11], v[64:65], v[10:11] op_sel_hi:[0,1]
	v_pk_mul_f32 v[8:9], v[64:65], v[8:9] op_sel_hi:[0,1]
	v_pk_mul_f32 v[6:7], v[64:65], v[6:7] op_sel_hi:[0,1]
	v_pk_mul_f32 v[4:5], v[64:65], v[4:5] op_sel_hi:[0,1]
	v_pk_mul_f32 v[2:3], v[64:65], v[2:3] op_sel_hi:[0,1]
	v_pk_mul_f32 v[0:1], v[64:65], v[0:1] op_sel_hi:[0,1]
	v_cvt_pk_f16_f32 v33, v46, v47
	v_cvt_f32_f16_e32 v34, v33
	s_waitcnt lgkmcnt(3)
	v_mfma_f32_32x32x16_f16 v[0:15], v[92:95], v[58:61], v[0:15]
	v_cvt_f32_f16_sdwa v35, v33 dst_sel:DWORD dst_unused:UNUSED_PAD src0_sel:WORD_1
	v_cvt_pk_f16_f32 v72, v124, v125
	v_cvt_f32_f16_e32 v62, v62
	v_cvt_f32_f16_e32 v63, v63
	v_add_f32_e64 v34, v46, -v34
	v_add_f32_e64 v35, v47, -v35
	v_cvt_f16_f32_e32 v87, v128
	v_sub_f32_e32 v62, v126, v62
	v_mfma_f32_32x32x16_f16 v[16:31], v[80:83], v[72:75], v[16:31]
	v_sub_f32_e32 v63, v127, v63
	v_cvt_pk_f16_f32 v85, v34, v35
	v_cvt_pk_f16_f32 v34, v48, v49
	v_cvt_pk_f16_f32 v84, v62, v63
	v_cvt_f32_f16_e32 v62, v34
	v_cvt_f32_f16_sdwa v63, v34 dst_sel:DWORD dst_unused:UNUSED_PAD src0_sel:WORD_1
	v_cvt_pk_f16_f32 v35, v50, v51
	v_cvt_f32_f16_e32 v102, v35
	v_cvt_f32_f16_sdwa v103, v35 dst_sel:DWORD dst_unused:UNUSED_PAD src0_sel:WORD_1
	v_mfma_f32_32x32x16_f16 v[0:15], v[92:95], v[68:71], v[0:15]
	v_cvt_f16_f32_e32 v68, v129
	v_add_f32_e64 v62, v48, -v62
	v_add_f32_e64 v63, v49, -v63
	v_cvt_pk_f16_f32 v69, v52, v53
	v_cvt_pk_f16_f32 v86, v62, v63
	v_pk_add_f32 v[62:63], v[50:51], v[102:103] neg_lo:[0,1] neg_hi:[0,1]
	v_cvt_f32_f16_e32 v102, v87
	v_cvt_f32_f16_e32 v71, v68
	v_mfma_f32_32x32x16_f16 v[16:31], v[80:83], v[76:79], v[16:31]
	v_cvt_pk_f16_f32 v87, v62, v63
	v_cvt_f32_f16_e32 v62, v69
	v_cvt_f32_f16_sdwa v63, v69 dst_sel:DWORD dst_unused:UNUSED_PAD src0_sel:WORD_1
	v_sub_f32_e32 v70, v128, v102
	v_cvt_pk_f16_f32 v32, v126, v127
	v_add_u32_e32 v103, 0xea40, v120
	v_cvt_pk_f16_f32 v68, v128, v129
	s_waitcnt lgkmcnt(1)
	v_mfma_f32_32x32x16_f16 v[0:15], v[108:111], v[58:61], v[0:15]
	v_sub_f32_e32 v58, v129, v71
	v_cvt_pk_f16_f32 v58, v70, v58
	v_add_f32_e64 v60, v52, -v62
	v_add_f32_e64 v61, v53, -v63
	v_cvt_pk_f16_f32 v70, v54, v55
	v_cvt_pk_f16_f32 v71, v56, v57
	v_cvt_pk_f16_f32 v59, v60, v61
	v_cvt_f32_f16_e32 v60, v70
	v_cvt_f32_f16_sdwa v61, v70 dst_sel:DWORD dst_unused:UNUSED_PAD src0_sel:WORD_1
	v_cvt_f32_f16_e32 v62, v71
	v_cvt_f32_f16_sdwa v63, v71 dst_sel:DWORD dst_unused:UNUSED_PAD src0_sel:WORD_1
	v_mfma_f32_32x32x16_f16 v[16:31], v[88:91], v[72:75], v[16:31]
	v_add_f32_e64 v60, v54, -v60
	v_add_f32_e64 v61, v55, -v61
	ds_read_b128 v[80:83], v120 offset:55360
	ds_read_b128 v[92:95], v120 offset:55392
	ds_read_b128 v[108:111], v120 offset:64576
	ds_read_b128 v[116:119], v120 offset:64608
	v_pk_add_f32 v[62:63], v[56:57], v[62:63] neg_lo:[0,1] neg_hi:[0,1]
	v_cvt_pk_f16_f32 v60, v60, v61
	v_cvt_pk_f16_f32 v61, v62, v63
	v_add_f32_e32 v63, 0, v65
	v_add_f32_e32 v63, v63, v101
	v_add_f32_e32 v63, v63, v66
	v_add_f32_e32 v63, v63, v67
	v_add_f32_e32 v36, v63, v36
	s_waitcnt lgkmcnt(3)
	v_mfma_f32_32x32x16_f16 v[16:31], v[80:83], v[32:35], v[16:31]
	v_add_f32_e32 v36, v36, v37
	v_add_f32_e32 v36, v36, v38
	v_add_f32_e32 v36, v36, v39
	v_add_f32_e32 v36, v36, v124
	v_add_f32_e32 v36, v36, v125
	v_add_f32_e32 v36, v36, v40
	v_add_f32_e32 v36, v36, v41
	v_mfma_f32_32x32x16_f16 v[0:15], v[96:99], v[72:75], v[0:15]
	v_add_f32_e32 v36, v36, v42
	v_add_f32_e32 v36, v36, v43
	v_add_f32_e32 v36, v36, v44
	v_add_f32_e32 v36, v36, v45
	v_add_f32_e32 v36, v36, v126
	v_add_f32_e32 v36, v36, v127
	v_add_f32_e32 v36, v36, v46
	v_mfma_f32_32x32x16_f16 v[16:31], v[80:83], v[84:87], v[16:31]
	v_add_f32_e32 v36, v36, v47
	v_add_f32_e32 v36, v36, v48
	v_add_f32_e32 v36, v36, v49
	v_add_f32_e32 v36, v36, v50
	v_add_f32_e32 v36, v36, v51
	v_add_f32_e32 v36, v36, v128
	v_add_f32_e32 v36, v36, v129
	v_mfma_f32_32x32x16_f16 v[0:15], v[96:99], v[76:79], v[0:15]
	v_add_f32_e32 v36, v36, v52
	v_add_u32_e32 v62, 0xea60, v120
	ds_read_b128 v[88:91], v120 offset:59968
	ds_read_b128 v[120:123], v120 offset:60000
	v_add_f32_e32 v36, v36, v53
	v_add_f32_e32 v36, v36, v54
	v_add_f32_e32 v36, v36, v55
	v_add_f32_e32 v36, v36, v56
	s_waitcnt lgkmcnt(3)
	v_mfma_f32_32x32x16_f16 v[16:31], v[108:111], v[32:35], v[16:31]
	v_add_f32_e32 v44, v36, v57
	v_fmac_f32_e32 v44, v100, v64
	ds_bpermute_b32 v45, v107, v44
	ds_read_b128 v[36:39], v103 offset:9216
	ds_read_b128 v[40:43], v62 offset:9216
	s_waitcnt lgkmcnt(0)
	s_barrier
	v_mfma_f32_32x32x16_f16 v[0:15], v[112:115], v[72:75], v[0:15]
	v_add_f32_e32 v44, v44, v45
	v_div_scale_f32 v45, s[4:5], v44, v44, 4.0
	v_rcp_f32_e32 v46, v45
	s_nop 0
	v_fma_f32 v47, -v45, v46, 1.0
	v_mfma_f32_32x32x16_f16 v[16:31], v[92:95], v[68:71], v[16:31]
	v_fmac_f32_e32 v46, v47, v46
	v_div_scale_f32 v47, vcc, 4.0, v44, 4.0
	v_mul_f32_e32 v48, v47, v46
	v_fma_f32 v49, -v45, v48, v47
	v_fmac_f32_e32 v48, v49, v46
	v_fma_f32 v45, -v45, v48, v47
	v_mfma_f32_32x32x16_f16 v[0:15], v[88:91], v[32:35], v[0:15]
	v_div_fmas_f32 v45, v45, v46, v48
	v_div_fixup_f32 v44, v45, v44, 4.0
	v_or3_b32 v47, s1, 0, 0
	v_or3_b32 v46, s0, v106, v104
	s_lshl_b32 s0, s2, 7
	v_lshlrev_b64 v[46:47], 10, v[46:47]
	s_and_b32 s0, s0, 0x380
	v_mfma_f32_32x32x16_f16 v[16:31], v[92:95], v[58:61], v[16:31]
	v_or_b32_e32 v46, s0, v46
	v_lshl_add_u64 v[48:49], s[8:9], 0, v[46:47]
	v_lshl_add_u64 v[46:47], s[10:11], 0, v[46:47]
	v_mfma_f32_32x32x16_f16 v[0:15], v[88:91], v[84:87], v[0:15]
	v_mfma_f32_32x32x16_f16 v[16:31], v[116:119], v[68:71], v[16:31]
	v_mfma_f32_32x32x16_f16 v[0:15], v[36:39], v[32:35], v[0:15]
	s_nop 10
	v_mul_f32_e32 v45, v44, v16
	v_fma_mixlo_f16 v50, v44, v16, 0
	v_fma_mixlo_f16 v16, v44, v16, -v50 op_sel_hi:[0,0,1]
	v_mul_f32_e64 v50, v44, v18
	v_mul_f32_e64 v51, v44, v19
	v_cvt_pk_f16_f32 v51, v50, v51
	v_cvt_f32_f16_e32 v52, v51
	v_cvt_f32_f16_sdwa v53, v51 dst_sel:DWORD dst_unused:UNUSED_PAD src0_sel:WORD_1
	v_mfma_f32_32x32x16_f16 v[0:15], v[120:123], v[68:71], v[0:15]
	v_mul_f32_e64 v32, v44, v22
	v_mul_f32_e64 v33, v44, v23
	v_fma_mixlo_f16 v55, v44, v17, 0
	v_fma_f32 v18, v44, v18, -v52
	v_fma_f32 v19, v44, v19, -v53
	v_cvt_pk_f16_f32 v33, v32, v33
	v_mul_f32_e32 v54, v44, v17
	v_fma_mixhi_f16 v16, v44, v17, -v55 op_sel_hi:[0,0,1]
	v_cvt_pk_f16_f32 v17, v18, v19
	v_lshlrev_b32_e32 v18, 3, v105
	v_mov_b32_e32 v19, 0
	v_cvt_f32_f16_e32 v34, v33
	v_cvt_f32_f16_sdwa v35, v33 dst_sel:DWORD dst_unused:UNUSED_PAD src0_sel:WORD_1
	v_lshl_add_u64 v[48:49], v[48:49], 0, v[18:19]
	v_lshl_add_u64 v[18:19], v[46:47], 0, v[18:19]
	global_store_dwordx2 v[18:19], v[16:17], off
	v_fma_mixlo_f16 v16, v44, v20, 0
	v_mul_f32_e32 v17, v44, v20
	v_fma_mixlo_f16 v16, v44, v20, -v16 op_sel_hi:[0,0,1]
	v_mul_f32_e32 v20, v44, v21
	v_fma_mixlo_f16 v36, v44, v21, 0
	v_mfma_f32_32x32x16_f16 v[0:15], v[120:123], v[58:61], v[0:15]
	v_cvt_pk_f16_f32 v32, v17, v20
	v_fma_mixhi_f16 v16, v44, v21, -v36 op_sel_hi:[0,0,1]
	v_fma_f32 v20, v44, v22, -v34
	v_fma_f32 v21, v44, v23, -v35
	v_cvt_pk_f16_f32 v17, v20, v21
	v_pk_mul_f32 v[20:21], v[44:45], v[26:27] op_sel_hi:[0,1]
	v_cvt_pk_f16_f32 v21, v20, v21
	v_cvt_f32_f16_e32 v22, v21
	v_cvt_f32_f16_sdwa v23, v21 dst_sel:DWORD dst_unused:UNUSED_PAD src0_sel:WORD_1
	v_cvt_pk_f16_f32 v50, v45, v54
	global_store_dwordx2 v[48:49], v[50:51], off
	global_store_dwordx2 v[48:49], v[32:33], off offset:16
	global_store_dwordx2 v[18:19], v[16:17], off offset:16
	v_fma_mixlo_f16 v16, v44, v24, 0
	v_mul_f32_e32 v17, v44, v24
	v_fma_mixlo_f16 v16, v44, v24, -v16 op_sel_hi:[0,0,1]
	v_mul_f32_e32 v24, v44, v25
	v_mfma_f32_32x32x16_f16 v[0:15], v[40:43], v[68:71], v[0:15]
	v_fma_mixlo_f16 v32, v44, v25, 0
	v_cvt_pk_f16_f32 v20, v17, v24
	v_fma_f32 v22, v44, v26, -v22
	v_fma_f32 v23, v44, v27, -v23
	v_fma_mixhi_f16 v16, v44, v25, -v32 op_sel_hi:[0,0,1]
	v_cvt_pk_f16_f32 v17, v22, v23
	global_store_dwordx2 v[48:49], v[20:21], off offset:32
	global_store_dwordx2 v[18:19], v[16:17], off offset:32
	v_pk_mul_f32 v[20:21], v[44:45], v[30:31] op_sel_hi:[0,1]
	v_cvt_pk_f16_f32 v21, v20, v21
	v_cvt_f32_f16_e32 v22, v21
	v_cvt_f32_f16_sdwa v23, v21 dst_sel:DWORD dst_unused:UNUSED_PAD src0_sel:WORD_1
	v_fma_mixlo_f16 v16, v44, v28, 0
	v_mul_f32_e32 v17, v44, v28
	v_fma_mixlo_f16 v16, v44, v28, -v16 op_sel_hi:[0,0,1]
	v_mul_f32_e32 v24, v44, v29
	v_fma_mixlo_f16 v25, v44, v29, 0
	v_cvt_pk_f16_f32 v20, v17, v24
	v_fma_mixhi_f16 v16, v44, v29, -v25 op_sel_hi:[0,0,1]
	v_pk_fma_f32 v[22:23], v[44:45], v[30:31], v[22:23] op_sel_hi:[0,1,1] neg_lo:[0,0,1] neg_hi:[0,0,1]
	v_cvt_pk_f16_f32 v17, v22, v23
	global_store_dwordx2 v[48:49], v[20:21], off offset:48
	global_store_dwordx2 v[18:19], v[16:17], off offset:48
	v_fma_mixlo_f16 v16, v44, v0, 0
	v_mul_f32_e32 v22, v44, v0
	v_fma_mixlo_f16 v0, v44, v0, -v16 op_sel_hi:[0,0,1]
	v_pk_mul_f32 v[16:17], v[44:45], v[2:3] op_sel_hi:[0,1]
	v_cvt_pk_f16_f32 v17, v16, v17
	v_cvt_f32_f16_e32 v20, v17
	v_cvt_f32_f16_sdwa v21, v17 dst_sel:DWORD dst_unused:UNUSED_PAD src0_sel:WORD_1
	v_fma_mixlo_f16 v24, v44, v1, 0
	v_mul_f32_e32 v23, v44, v1
	v_fma_mixhi_f16 v0, v44, v1, -v24 op_sel_hi:[0,0,1]
	v_pk_fma_f32 v[2:3], v[44:45], v[2:3], v[20:21] op_sel_hi:[0,1,1] neg_lo:[0,0,1] neg_hi:[0,0,1]
	v_cvt_pk_f16_f32 v1, v2, v3
	v_pk_mul_f32 v[2:3], v[44:45], v[6:7] op_sel_hi:[0,1]
	v_cvt_pk_f16_f32 v16, v22, v23
	v_cvt_pk_f16_f32 v3, v2, v3
	global_store_dwordx2 v[48:49], v[16:17], off offset:64
	global_store_dwordx2 v[18:19], v[0:1], off offset:64
	v_cvt_f32_f16_e32 v16, v3
	v_cvt_f32_f16_sdwa v17, v3 dst_sel:DWORD dst_unused:UNUSED_PAD src0_sel:WORD_1
	v_fma_mixlo_f16 v0, v44, v4, 0
	v_mul_f32_e32 v1, v44, v4
	v_fma_mixlo_f16 v0, v44, v4, -v0 op_sel_hi:[0,0,1]
	v_mul_f32_e32 v4, v44, v5
	v_fma_mixlo_f16 v20, v44, v5, 0
	v_cvt_pk_f16_f32 v2, v1, v4
	v_fma_mixhi_f16 v0, v44, v5, -v20 op_sel_hi:[0,0,1]
	v_pk_fma_f32 v[4:5], v[44:45], v[6:7], v[16:17] op_sel_hi:[0,1,1] neg_lo:[0,0,1] neg_hi:[0,0,1]
	v_cvt_pk_f16_f32 v1, v4, v5
	global_store_dwordx2 v[48:49], v[2:3], off offset:80
	global_store_dwordx2 v[18:19], v[0:1], off offset:80
	v_pk_mul_f32 v[2:3], v[44:45], v[10:11] op_sel_hi:[0,1]
	v_cvt_pk_f16_f32 v3, v2, v3
	v_cvt_f32_f16_e32 v4, v3
	v_cvt_f32_f16_sdwa v5, v3 dst_sel:DWORD dst_unused:UNUSED_PAD src0_sel:WORD_1
	v_mul_f32_e32 v1, v44, v8
	v_fma_mixlo_f16 v0, v44, v8, 0
	v_mul_f32_e32 v6, v44, v9
	v_fma_mixlo_f16 v0, v44, v8, -v0 op_sel_hi:[0,0,1]
	v_fma_mixlo_f16 v7, v44, v9, 0
	v_cvt_pk_f16_f32 v2, v1, v6
	v_pk_fma_f32 v[4:5], v[44:45], v[10:11], v[4:5] op_sel_hi:[0,1,1] neg_lo:[0,0,1] neg_hi:[0,0,1]
	v_fma_mixhi_f16 v0, v44, v9, -v7 op_sel_hi:[0,0,1]
	v_cvt_pk_f16_f32 v1, v4, v5
	global_store_dwordx2 v[48:49], v[2:3], off offset:96
	global_store_dwordx2 v[18:19], v[0:1], off offset:96
	v_pk_mul_f32 v[2:3], v[44:45], v[14:15] op_sel_hi:[0,1]
	v_cvt_pk_f16_f32 v3, v2, v3
	v_cvt_f32_f16_e32 v4, v3
	v_cvt_f32_f16_sdwa v5, v3 dst_sel:DWORD dst_unused:UNUSED_PAD src0_sel:WORD_1
	v_mul_f32_e32 v1, v44, v12
	v_fma_mixlo_f16 v0, v44, v12, 0
	v_mul_f32_e32 v6, v44, v13
	v_fma_mixlo_f16 v0, v44, v12, -v0 op_sel_hi:[0,0,1]
	v_fma_mixlo_f16 v7, v44, v13, 0
	v_cvt_pk_f16_f32 v2, v1, v6
	v_pk_fma_f32 v[4:5], v[44:45], v[14:15], v[4:5] op_sel_hi:[0,1,1] neg_lo:[0,0,1] neg_hi:[0,0,1]
	v_fma_mixhi_f16 v0, v44, v13, -v7 op_sel_hi:[0,0,1]
	v_cvt_pk_f16_f32 v1, v4, v5
	global_store_dwordx2 v[48:49], v[2:3], off offset:112
	global_store_dwordx2 v[18:19], v[0:1], off offset:112
	s_endpgm
	.p2alignl 8, 3212836864
